# fused LSTM: x fragments reloaded right after their last use (5 steps of prefetch slack instead of 2.5); nt message stores in MP kernels
# speedup vs baseline: 1.0240x; 1.0141x over previous
_Z12lstm2_kernelPKDF16_PKDv8_DF16_Pf:
	s_load_dwordx4 s[8:11], s[0:1], 0x0
	s_load_dwordx2 s[12:13], s[0:1], 0x10
	s_and_b32 s14, s2, 1
	s_lshr_b32 s15, s2, 1
	v_and_b32_e32 v1, 63, v0
	v_lshrrev_b32_e32 v2, 6, v0
	v_lshrrev_b32_e32 v3, 4, v1
	v_and_b32_e32 v4, 15, v0
	v_lshrrev_b32_e32 v5, 2, v4
	v_and_b32_e32 v6, 3, v0
	v_lshlrev_b32_e32 v7, 4, v1
	v_lshl_add_u32 v8, v2, 13, v7
	v_lshl_add_u32 v9, v2, 14, v7
	s_waitcnt lgkmcnt(0)
	s_lshl_b32 s16, s14, 15
	s_add_u32 s16, s16, 0x64000
	s_add_u32 s16, s10, s16
	s_addc_u32 s17, s11, 0
	s_lshl_b32 s18, s14, 16
	s_add_u32 s18, s18, 0x44000
	s_add_u32 s18, s10, s18
	s_addc_u32 s19, s11, 0
	v_add_u32_e32 v10, 0x1000, v8
	global_load_dwordx4 v[16:19], v8, s[16:17] offset:0
	global_load_dwordx4 v[20:23], v8, s[16:17] offset:1024
	global_load_dwordx4 v[24:27], v8, s[16:17] offset:2048
	global_load_dwordx4 v[28:31], v8, s[16:17] offset:3072
	global_load_dwordx4 v[32:35], v10, s[16:17] offset:0
	global_load_dwordx4 v[36:39], v10, s[16:17] offset:1024
	global_load_dwordx4 v[40:43], v10, s[16:17] offset:2048
	global_load_dwordx4 v[44:47], v10, s[16:17] offset:3072
	v_add_u32_e32 v11, 0x1000, v9
	v_add_u32_e32 v12, 0x2000, v9
	v_add_u32_e32 v13, 0x3000, v9
	global_load_dwordx4 v[48:51], v9, s[18:19] offset:0
	global_load_dwordx4 v[52:55], v9, s[18:19] offset:1024
	global_load_dwordx4 v[56:59], v9, s[18:19] offset:2048
	global_load_dwordx4 v[60:63], v9, s[18:19] offset:3072
	global_load_dwordx4 v[64:67], v11, s[18:19] offset:0
	global_load_dwordx4 v[68:71], v11, s[18:19] offset:1024
	global_load_dwordx4 v[72:75], v11, s[18:19] offset:2048
	global_load_dwordx4 v[76:79], v11, s[18:19] offset:3072
	global_load_dwordx4 v[80:83], v12, s[18:19] offset:0
	global_load_dwordx4 v[84:87], v12, s[18:19] offset:1024
	global_load_dwordx4 v[88:91], v12, s[18:19] offset:2048
	global_load_dwordx4 v[92:95], v12, s[18:19] offset:3072
	global_load_dwordx4 v[96:99], v13, s[18:19] offset:0
	global_load_dwordx4 v[100:103], v13, s[18:19] offset:1024
	global_load_dwordx4 v[104:107], v13, s[18:19] offset:2048
	global_load_dwordx4 v[108:111], v13, s[18:19] offset:3072
	s_lshl_b32 s22, s14, 10
	s_add_u32 s22, s8, s22
	s_addc_u32 s23, s9, 0
	v_lshl_add_u32 v14, v2, 4, v3
	v_lshlrev_b32_e32 v14, 2, v14
	global_load_dword v112, v14, s[22:23] offset:0
	global_load_dword v113, v14, s[22:23] offset:256
	global_load_dword v114, v14, s[22:23] offset:512
	global_load_dword v115, v14, s[22:23] offset:768
	global_load_dword v116, v14, s[22:23] offset:16
	global_load_dword v117, v14, s[22:23] offset:272
	global_load_dword v118, v14, s[22:23] offset:528
	global_load_dword v119, v14, s[22:23] offset:784
	global_load_dword v120, v14, s[22:23] offset:32
	global_load_dword v121, v14, s[22:23] offset:288
	global_load_dword v122, v14, s[22:23] offset:544
	global_load_dword v123, v14, s[22:23] offset:800
	global_load_dword v124, v14, s[22:23] offset:48
	global_load_dword v125, v14, s[22:23] offset:304
	global_load_dword v126, v14, s[22:23] offset:560
	global_load_dword v127, v14, s[22:23] offset:816
	s_add_u32 s24, s8, 0xc808000
	s_addc_u32 s25, s9, 0
	s_lshl_b32 s26, s15, 2
	v_add_u32_e32 v15, s26, v6
	s_cmp_eq_u32 s14, 0
	v_sub_u32_e32 v200, 0x18f, v5
	s_cselect_b64 vcc, -1, 0
	s_nop 1
	v_cndmask_b32_e32 v200, v200, v5, vcc
	v_mov_b32_e32 v201, 0x190
	v_mad_u32_u24 v200, v15, v201, v200
	v_lshlrev_b32_e32 v200, 8, v200
	v_lshl_add_u32 v200, v3, 4, v200
	v_mov_b32_e32 v201, 0
	v_lshl_add_u64 v[228:229], s[24:25], 0, v[200:201]
	s_mov_b32 s28, 0x400
	s_cselect_b32 s20, s28, 0xfffffc00
	s_cselect_b32 s21, 0, -1
	global_load_dwordx4 v[128:131], v[228:229], off offset:0
	global_load_dwordx4 v[132:135], v[228:229], off offset:64
	global_load_dwordx4 v[136:139], v[228:229], off offset:128
	global_load_dwordx4 v[140:143], v[228:229], off offset:192
	v_lshl_add_u64 v[228:229], v[228:229], 0, s[20:21]
	global_load_dwordx4 v[144:147], v[228:229], off offset:0
	global_load_dwordx4 v[148:151], v[228:229], off offset:64
	global_load_dwordx4 v[152:155], v[228:229], off offset:128
	global_load_dwordx4 v[156:159], v[228:229], off offset:192
	v_lshl_add_u64 v[228:229], v[228:229], 0, s[20:21]
	v_mul_u32_u24_e32 v202, 144, v6
	v_lshl_add_u32 v224, v3, 4, v202
	v_lshl_add_u32 v203, v2, 4, v3
	v_lshl_add_u32 v203, v5, 2, v203
	v_lshl_add_u32 v225, v203, 1, v202
	v_mul_u32_u24_e32 v204, 8704, v2
	v_lshlrev_b32_e32 v205, 8, v3
	v_lshl_add_u32 v205, v6, 4, v205
	v_add_u32_e32 v205, 1280, v205
	v_add_u32_e32 v205, v205, v204
	v_lshl_add_u32 v226, v5, 6, v205
	v_mul_u32_u24_e32 v206, 1088, v5
	v_add_u32_e32 v227, v205, v206
	v_lshlrev_b32_e32 v206, 4, v3
	v_cmp_gt_u32_e32 vcc, 2, v5
	s_nop 1
	v_add_u32_e32 v208, 1152, v206
	v_cndmask_b32_e32 v209, v208, v224, vcc
	v_cndmask_b32_e32 v211, v224, v208, vcc
	v_add_u32_e32 v208, 576, v206
	v_cndmask_b32_e32 v210, v208, v224, vcc
	v_cndmask_b32_e32 v212, v224, v208, vcc
	s_lshl_b32 s27, s14, 6
	v_lshl_add_u32 v230, v15, 7, v203
	v_add_u32_e32 v230, s27, v230
	v_lshlrev_b32_e32 v230, 2, v230
	v_mov_b32_e32 v208, 0
	v_lshlrev_b32_e32 v200, 2, v0
	v_lshlrev_b32_e32 v201, 2, v1
	ds_write_b32 v200, v208
	ds_write_b32 v201, v208 offset:1024
	v_mov_b32_e32 v220, 0
	v_mov_b32_e32 v221, 0xff61b1e6
	v_mov_b32_e32 v222, 0x4038aa3b
	v_mov_b32_e32 v215, 0xff61b1e6
	s_waitcnt vmcnt(0)
	v_mfma_f32_16x16x32_f16 v[168:171], v[48:51], v[128:131], v[112:115]
	v_mfma_f32_16x16x32_f16 v[168:171], v[52:55], v[132:135], v[168:171]
	v_mfma_f32_16x16x32_f16 v[168:171], v[56:59], v[136:139], v[168:171]
	v_mfma_f32_16x16x32_f16 v[168:171], v[60:63], v[140:143], v[168:171]
	v_mfma_f32_16x16x32_f16 v[172:175], v[64:67], v[128:131], v[116:119]
	v_mfma_f32_16x16x32_f16 v[172:175], v[68:71], v[132:135], v[172:175]
	v_mfma_f32_16x16x32_f16 v[172:175], v[72:75], v[136:139], v[172:175]
	v_mfma_f32_16x16x32_f16 v[172:175], v[76:79], v[140:143], v[172:175]
	v_mfma_f32_16x16x32_f16 v[176:179], v[80:83], v[128:131], v[120:123]
	v_mfma_f32_16x16x32_f16 v[176:179], v[84:87], v[132:135], v[176:179]
	v_mfma_f32_16x16x32_f16 v[176:179], v[88:91], v[136:139], v[176:179]
	v_mfma_f32_16x16x32_f16 v[176:179], v[92:95], v[140:143], v[176:179]
	v_mfma_f32_16x16x32_f16 v[180:183], v[96:99], v[128:131], v[124:127]
	v_mfma_f32_16x16x32_f16 v[180:183], v[100:103], v[132:135], v[180:183]
	v_mfma_f32_16x16x32_f16 v[180:183], v[104:107], v[136:139], v[180:183]
	v_mfma_f32_16x16x32_f16 v[180:183], v[108:111], v[140:143], v[180:183]
	v_mfma_f32_16x16x32_f16 v[160:163], v[48:51], v[144:147], v[112:115]
	v_mfma_f32_16x16x32_f16 v[164:167], v[64:67], v[144:147], v[116:119]
	v_mfma_f32_16x16x32_f16 v[160:163], v[52:55], v[148:151], v[160:163]
	v_mfma_f32_16x16x32_f16 v[160:163], v[56:59], v[152:155], v[160:163]
	s_nop 7
	ds_write_b128 v227, v[168:171] offset:0
	ds_write_b128 v227, v[172:175] offset:64
	ds_write_b128 v227, v[176:179] offset:128
	ds_write_b128 v227, v[180:183] offset:192
	global_load_dwordx4 v[128:131], v[228:229], off offset:0
	global_load_dwordx4 v[132:135], v[228:229], off offset:64
	global_load_dwordx4 v[136:139], v[228:229], off offset:128
	global_load_dwordx4 v[140:143], v[228:229], off offset:192
	v_lshl_add_u64 v[228:229], v[228:229], 0, s[20:21]
	s_movk_i32 s4, 50
	s_waitcnt lgkmcnt(0)
	s_barrier
	ds_read_b128 v[192:195], v226 offset:0
.Llstm3_loop:
	ds_read_b128 v[184:187], v209 offset:0
	ds_read_b128 v[188:191], v209 offset:64
	ds_read_b128 v[176:179], v211 offset:0
	ds_read_b128 v[180:183], v211 offset:64
	v_mfma_f32_16x16x32_f16 v[164:167], v[68:71], v[148:151], v[164:167]
	s_waitcnt vmcnt(4)
	v_mfma_f32_16x16x32_f16 v[160:163], v[60:63], v[156:159], v[160:163]
	s_waitcnt lgkmcnt(3)
	v_mfma_f32_16x16x32_f16 v[168:171], v[16:19], v[184:187], v[192:195]
	v_mfma_f32_16x16x32_f16 v[172:175], v[24:27], v[184:187], v[192:195]
	s_waitcnt lgkmcnt(2)
	v_mfma_f32_16x16x32_f16 v[168:171], v[20:23], v[188:191], v[168:171]
	v_mfma_f32_16x16x32_f16 v[172:175], v[28:31], v[188:191], v[172:175]
	s_waitcnt lgkmcnt(1)
	v_mfma_f32_16x16x32_f16 v[168:171], v[32:35], v[176:179], v[168:171]
	v_mfma_f32_16x16x32_f16 v[172:175], v[40:43], v[176:179], v[172:175]
	s_waitcnt lgkmcnt(0)
	v_mfma_f32_16x16x32_f16 v[168:171], v[36:39], v[180:183], v[168:171]
	v_mfma_f32_16x16x32_f16 v[172:175], v[44:47], v[180:183], v[172:175]
	v_max_f32_e32 v221, v221, v215
	s_nop 6
	v_mov_b32_dpp v168, v172 quad_perm:[0,1,2,3] row_mask:0xf bank_mask:0xa
	v_mov_b32_dpp v169, v173 quad_perm:[0,1,2,3] row_mask:0xf bank_mask:0xa
	v_mov_b32_dpp v170, v174 quad_perm:[0,1,2,3] row_mask:0xf bank_mask:0xa
	v_exp_f32_e32 v200, v168
	v_mov_b32_dpp v171, v175 quad_perm:[0,1,2,3] row_mask:0xf bank_mask:0xa
	v_exp_f32_e32 v201, v169
	v_exp_f32_e32 v202, v170
	v_add_f32_e32 v200, 1.0, v200
	v_exp_f32_e32 v203, v171
	v_add_f32_e32 v201, 1.0, v201
	v_add_f32_e32 v202, 1.0, v202
	v_rcp_f32_e32 v202, v202
	v_rcp_f32_e32 v200, v200
	v_rcp_f32_e32 v201, v201
	v_add_f32_e32 v203, 1.0, v203
	v_fmamk_f32 v204, v202, 0xc0b8aa3b, v222
	v_rcp_f32_e32 v203, v203
	v_mul_f32_e32 v205, v200, v204
	v_fma_f32 v220, v201, v220, v205
	v_exp_f32_e32 v206, v220
	v_mul_f32_e32 v207, -2.0, v203
	v_add_f32_e32 v206, 1.0, v206
	v_rcp_f32_e32 v206, v206
	s_nop 0
	v_fma_mixlo_f16 v208, v206, v207, v203
	ds_write_b16 v225, v208 offset:576
	v_fma_f32 v215, v206, v207, v203
	v_mfma_f32_16x16x32_f16 v[232:235], v[80:83], v[144:147], v[120:123]
	v_mfma_f32_16x16x32_f16 v[164:167], v[72:75], v[152:155], v[164:167]
	ds_write_b128 v227, v[160:163] offset:4352
	ds_read_b128 v[196:199], v226 offset:1088
	s_waitcnt lgkmcnt(2)
	s_barrier
	ds_read_b128 v[184:187], v210 offset:576
	ds_read_b128 v[188:191], v210 offset:640
	ds_read_b128 v[176:179], v212 offset:576
	ds_read_b128 v[180:183], v212 offset:640
	v_mfma_f32_16x16x32_f16 v[232:235], v[84:87], v[148:151], v[232:235]
	v_mfma_f32_16x16x32_f16 v[164:167], v[76:79], v[156:159], v[164:167]
	s_waitcnt lgkmcnt(3)
	v_mfma_f32_16x16x32_f16 v[168:171], v[16:19], v[184:187], v[196:199]
	v_mfma_f32_16x16x32_f16 v[172:175], v[24:27], v[184:187], v[196:199]
	s_waitcnt lgkmcnt(2)
	v_mfma_f32_16x16x32_f16 v[168:171], v[20:23], v[188:191], v[168:171]
	v_mfma_f32_16x16x32_f16 v[172:175], v[28:31], v[188:191], v[172:175]
	s_waitcnt lgkmcnt(1)
	v_mfma_f32_16x16x32_f16 v[168:171], v[32:35], v[176:179], v[168:171]
	v_mfma_f32_16x16x32_f16 v[172:175], v[40:43], v[176:179], v[172:175]
	s_waitcnt lgkmcnt(0)
	v_mfma_f32_16x16x32_f16 v[168:171], v[36:39], v[180:183], v[168:171]
	v_mfma_f32_16x16x32_f16 v[172:175], v[44:47], v[180:183], v[172:175]
	v_max_f32_e32 v221, v221, v215
	s_nop 6
	v_mov_b32_dpp v168, v172 quad_perm:[0,1,2,3] row_mask:0xf bank_mask:0xa
	v_mov_b32_dpp v169, v173 quad_perm:[0,1,2,3] row_mask:0xf bank_mask:0xa
	v_mov_b32_dpp v170, v174 quad_perm:[0,1,2,3] row_mask:0xf bank_mask:0xa
	v_exp_f32_e32 v200, v168
	v_mov_b32_dpp v171, v175 quad_perm:[0,1,2,3] row_mask:0xf bank_mask:0xa
	v_exp_f32_e32 v201, v169
	v_exp_f32_e32 v202, v170
	v_add_f32_e32 v200, 1.0, v200
	v_exp_f32_e32 v203, v171
	v_add_f32_e32 v201, 1.0, v201
	v_add_f32_e32 v202, 1.0, v202
	v_rcp_f32_e32 v202, v202
	v_rcp_f32_e32 v200, v200
	v_rcp_f32_e32 v201, v201
	v_add_f32_e32 v203, 1.0, v203
	v_fmamk_f32 v204, v202, 0xc0b8aa3b, v222
	v_rcp_f32_e32 v203, v203
	v_mul_f32_e32 v205, v200, v204
	v_fma_f32 v220, v201, v220, v205
	v_exp_f32_e32 v206, v220
	v_mul_f32_e32 v207, -2.0, v203
	v_add_f32_e32 v206, 1.0, v206
	v_rcp_f32_e32 v206, v206
	s_nop 0
	v_fma_mixlo_f16 v208, v206, v207, v203
	ds_write_b16 v225, v208 offset:0
	v_fma_f32 v215, v206, v207, v203
	v_mfma_f32_16x16x32_f16 v[236:239], v[96:99], v[144:147], v[124:127]
	v_mfma_f32_16x16x32_f16 v[232:235], v[88:91], v[152:155], v[232:235]
	global_load_dwordx4 v[144:147], v[228:229], off offset:0
	ds_write_b128 v227, v[164:167] offset:4416
	ds_read_b128 v[192:195], v226 offset:2176
	s_waitcnt lgkmcnt(2)
	s_barrier
	ds_read_b128 v[184:187], v209 offset:0
	ds_read_b128 v[188:191], v209 offset:64
	ds_read_b128 v[176:179], v211 offset:0
	ds_read_b128 v[180:183], v211 offset:64
	v_mfma_f32_16x16x32_f16 v[236:239], v[100:103], v[148:151], v[236:239]
	v_mfma_f32_16x16x32_f16 v[232:235], v[92:95], v[156:159], v[232:235]
	global_load_dwordx4 v[148:151], v[228:229], off offset:64
	s_waitcnt lgkmcnt(3)
	v_mfma_f32_16x16x32_f16 v[168:171], v[16:19], v[184:187], v[192:195]
	v_mfma_f32_16x16x32_f16 v[172:175], v[24:27], v[184:187], v[192:195]
	s_waitcnt lgkmcnt(2)
	v_mfma_f32_16x16x32_f16 v[168:171], v[20:23], v[188:191], v[168:171]
	v_mfma_f32_16x16x32_f16 v[172:175], v[28:31], v[188:191], v[172:175]
	s_waitcnt lgkmcnt(1)
	v_mfma_f32_16x16x32_f16 v[168:171], v[32:35], v[176:179], v[168:171]
	v_mfma_f32_16x16x32_f16 v[172:175], v[40:43], v[176:179], v[172:175]
	s_waitcnt lgkmcnt(0)
	v_mfma_f32_16x16x32_f16 v[168:171], v[36:39], v[180:183], v[168:171]
	v_mfma_f32_16x16x32_f16 v[172:175], v[44:47], v[180:183], v[172:175]
	v_max_f32_e32 v221, v221, v215
	s_nop 6
	v_mov_b32_dpp v168, v172 quad_perm:[0,1,2,3] row_mask:0xf bank_mask:0xa
	v_mov_b32_dpp v169, v173 quad_perm:[0,1,2,3] row_mask:0xf bank_mask:0xa
	v_mov_b32_dpp v170, v174 quad_perm:[0,1,2,3] row_mask:0xf bank_mask:0xa
	v_exp_f32_e32 v200, v168
	v_mov_b32_dpp v171, v175 quad_perm:[0,1,2,3] row_mask:0xf bank_mask:0xa
	v_exp_f32_e32 v201, v169
	v_exp_f32_e32 v202, v170
	v_add_f32_e32 v200, 1.0, v200
	v_exp_f32_e32 v203, v171
	v_add_f32_e32 v201, 1.0, v201
	v_add_f32_e32 v202, 1.0, v202
	v_rcp_f32_e32 v202, v202
	v_rcp_f32_e32 v200, v200
	v_rcp_f32_e32 v201, v201
	v_add_f32_e32 v203, 1.0, v203
	v_fmamk_f32 v204, v202, 0xc0b8aa3b, v222
	v_rcp_f32_e32 v203, v203
	v_mul_f32_e32 v205, v200, v204
	v_fma_f32 v220, v201, v220, v205
	v_exp_f32_e32 v206, v220
	v_mul_f32_e32 v207, -2.0, v203
	v_add_f32_e32 v206, 1.0, v206
	v_rcp_f32_e32 v206, v206
	s_nop 0
	v_fma_mixlo_f16 v208, v206, v207, v203
	ds_write_b16 v225, v208 offset:576
	v_fma_f32 v215, v206, v207, v203
	s_waitcnt vmcnt(5)
	v_mfma_f32_16x16x32_f16 v[160:163], v[48:51], v[128:131], v[112:115]
	v_mfma_f32_16x16x32_f16 v[236:239], v[104:107], v[152:155], v[236:239]
	global_load_dwordx4 v[152:155], v[228:229], off offset:128
	ds_write_b128 v227, v[232:235] offset:4480
	ds_read_b128 v[196:199], v226 offset:3264
	s_waitcnt lgkmcnt(2)
	s_barrier
	ds_read_b128 v[184:187], v210 offset:576
	ds_read_b128 v[188:191], v210 offset:640
	ds_read_b128 v[176:179], v212 offset:576
	ds_read_b128 v[180:183], v212 offset:640
	s_waitcnt vmcnt(5)
	v_mfma_f32_16x16x32_f16 v[160:163], v[52:55], v[132:135], v[160:163]
	v_mfma_f32_16x16x32_f16 v[236:239], v[108:111], v[156:159], v[236:239]
	global_load_dwordx4 v[156:159], v[228:229], off offset:192
	v_lshl_add_u64 v[228:229], v[228:229], 0, s[20:21]
	s_waitcnt lgkmcnt(3)
	v_mfma_f32_16x16x32_f16 v[168:171], v[16:19], v[184:187], v[196:199]
	v_mfma_f32_16x16x32_f16 v[172:175], v[24:27], v[184:187], v[196:199]
	s_waitcnt lgkmcnt(2)
	v_mfma_f32_16x16x32_f16 v[168:171], v[20:23], v[188:191], v[168:171]
	v_mfma_f32_16x16x32_f16 v[172:175], v[28:31], v[188:191], v[172:175]
	s_waitcnt lgkmcnt(1)
	v_mfma_f32_16x16x32_f16 v[168:171], v[32:35], v[176:179], v[168:171]
	v_mfma_f32_16x16x32_f16 v[172:175], v[40:43], v[176:179], v[172:175]
	s_waitcnt lgkmcnt(0)
	v_mfma_f32_16x16x32_f16 v[168:171], v[36:39], v[180:183], v[168:171]
	v_mfma_f32_16x16x32_f16 v[172:175], v[44:47], v[180:183], v[172:175]
	v_max_f32_e32 v221, v221, v215
	s_nop 6
	v_mov_b32_dpp v168, v172 quad_perm:[0,1,2,3] row_mask:0xf bank_mask:0xa
	v_mov_b32_dpp v169, v173 quad_perm:[0,1,2,3] row_mask:0xf bank_mask:0xa
	v_mov_b32_dpp v170, v174 quad_perm:[0,1,2,3] row_mask:0xf bank_mask:0xa
	v_exp_f32_e32 v200, v168
	v_mov_b32_dpp v171, v175 quad_perm:[0,1,2,3] row_mask:0xf bank_mask:0xa
	v_exp_f32_e32 v201, v169
	v_exp_f32_e32 v202, v170
	v_add_f32_e32 v200, 1.0, v200
	v_exp_f32_e32 v203, v171
	v_add_f32_e32 v201, 1.0, v201
	v_add_f32_e32 v202, 1.0, v202
	v_rcp_f32_e32 v202, v202
	v_rcp_f32_e32 v200, v200
	v_rcp_f32_e32 v201, v201
	v_add_f32_e32 v203, 1.0, v203
	v_fmamk_f32 v204, v202, 0xc0b8aa3b, v222
	v_rcp_f32_e32 v203, v203
	v_mul_f32_e32 v205, v200, v204
	v_fma_f32 v220, v201, v220, v205
	v_exp_f32_e32 v206, v220
	v_mul_f32_e32 v207, -2.0, v203
	v_add_f32_e32 v206, 1.0, v206
	v_rcp_f32_e32 v206, v206
	s_nop 0
	v_fma_mixlo_f16 v208, v206, v207, v203
	ds_write_b16 v225, v208 offset:0
	v_fma_f32 v215, v206, v207, v203
	v_mfma_f32_16x16x32_f16 v[164:167], v[64:67], v[128:131], v[116:119]
	s_waitcnt vmcnt(5)
	v_mfma_f32_16x16x32_f16 v[160:163], v[56:59], v[136:139], v[160:163]
	ds_write_b128 v227, v[236:239] offset:4544
	ds_read_b128 v[192:195], v226 offset:4352
	s_waitcnt lgkmcnt(2)
	s_barrier
	ds_read_b128 v[184:187], v209 offset:0
	ds_read_b128 v[188:191], v209 offset:64
	ds_read_b128 v[176:179], v211 offset:0
	ds_read_b128 v[180:183], v211 offset:64
	v_mfma_f32_16x16x32_f16 v[164:167], v[68:71], v[132:135], v[164:167]
	s_waitcnt vmcnt(4)
	v_mfma_f32_16x16x32_f16 v[160:163], v[60:63], v[140:143], v[160:163]
	s_waitcnt lgkmcnt(3)
	v_mfma_f32_16x16x32_f16 v[168:171], v[16:19], v[184:187], v[192:195]
	v_mfma_f32_16x16x32_f16 v[172:175], v[24:27], v[184:187], v[192:195]
	s_waitcnt lgkmcnt(2)
	v_mfma_f32_16x16x32_f16 v[168:171], v[20:23], v[188:191], v[168:171]
	v_mfma_f32_16x16x32_f16 v[172:175], v[28:31], v[188:191], v[172:175]
	s_waitcnt lgkmcnt(1)
	v_mfma_f32_16x16x32_f16 v[168:171], v[32:35], v[176:179], v[168:171]
	v_mfma_f32_16x16x32_f16 v[172:175], v[40:43], v[176:179], v[172:175]
	s_waitcnt lgkmcnt(0)
	v_mfma_f32_16x16x32_f16 v[168:171], v[36:39], v[180:183], v[168:171]
	v_mfma_f32_16x16x32_f16 v[172:175], v[44:47], v[180:183], v[172:175]
	v_max_f32_e32 v221, v221, v215
	s_nop 6
	v_mov_b32_dpp v168, v172 quad_perm:[0,1,2,3] row_mask:0xf bank_mask:0xa
	v_mov_b32_dpp v169, v173 quad_perm:[0,1,2,3] row_mask:0xf bank_mask:0xa
	v_mov_b32_dpp v170, v174 quad_perm:[0,1,2,3] row_mask:0xf bank_mask:0xa
	v_exp_f32_e32 v200, v168
	v_mov_b32_dpp v171, v175 quad_perm:[0,1,2,3] row_mask:0xf bank_mask:0xa
	v_exp_f32_e32 v201, v169
	v_exp_f32_e32 v202, v170
	v_add_f32_e32 v200, 1.0, v200
	v_exp_f32_e32 v203, v171
	v_add_f32_e32 v201, 1.0, v201
	v_add_f32_e32 v202, 1.0, v202
	v_rcp_f32_e32 v202, v202
	v_rcp_f32_e32 v200, v200
	v_rcp_f32_e32 v201, v201
	v_add_f32_e32 v203, 1.0, v203
	v_fmamk_f32 v204, v202, 0xc0b8aa3b, v222
	v_rcp_f32_e32 v203, v203
	v_mul_f32_e32 v205, v200, v204
	v_fma_f32 v220, v201, v220, v205
	v_exp_f32_e32 v206, v220
	v_mul_f32_e32 v207, -2.0, v203
	v_add_f32_e32 v206, 1.0, v206
	v_rcp_f32_e32 v206, v206
	s_nop 0
	v_fma_mixlo_f16 v208, v206, v207, v203
	ds_write_b16 v225, v208 offset:576
	v_fma_f32 v215, v206, v207, v203
	v_mfma_f32_16x16x32_f16 v[232:235], v[80:83], v[128:131], v[120:123]
	v_mfma_f32_16x16x32_f16 v[164:167], v[72:75], v[136:139], v[164:167]
	ds_write_b128 v227, v[160:163] offset:0
	ds_read_b128 v[196:199], v226 offset:5440
	s_waitcnt lgkmcnt(2)
	s_barrier
	ds_read_b128 v[184:187], v210 offset:576
	ds_read_b128 v[188:191], v210 offset:640
	ds_read_b128 v[176:179], v212 offset:576
	ds_read_b128 v[180:183], v212 offset:640
	v_mfma_f32_16x16x32_f16 v[232:235], v[84:87], v[132:135], v[232:235]
	v_mfma_f32_16x16x32_f16 v[164:167], v[76:79], v[140:143], v[164:167]
	s_waitcnt lgkmcnt(3)
	v_mfma_f32_16x16x32_f16 v[168:171], v[16:19], v[184:187], v[196:199]
	v_mfma_f32_16x16x32_f16 v[172:175], v[24:27], v[184:187], v[196:199]
	s_waitcnt lgkmcnt(2)
	v_mfma_f32_16x16x32_f16 v[168:171], v[20:23], v[188:191], v[168:171]
	v_mfma_f32_16x16x32_f16 v[172:175], v[28:31], v[188:191], v[172:175]
	s_waitcnt lgkmcnt(1)
	v_mfma_f32_16x16x32_f16 v[168:171], v[32:35], v[176:179], v[168:171]
	v_mfma_f32_16x16x32_f16 v[172:175], v[40:43], v[176:179], v[172:175]
	s_waitcnt lgkmcnt(0)
	v_mfma_f32_16x16x32_f16 v[168:171], v[36:39], v[180:183], v[168:171]
	v_mfma_f32_16x16x32_f16 v[172:175], v[44:47], v[180:183], v[172:175]
	v_max_f32_e32 v221, v221, v215
	s_nop 6
	v_mov_b32_dpp v168, v172 quad_perm:[0,1,2,3] row_mask:0xf bank_mask:0xa
	v_mov_b32_dpp v169, v173 quad_perm:[0,1,2,3] row_mask:0xf bank_mask:0xa
	v_mov_b32_dpp v170, v174 quad_perm:[0,1,2,3] row_mask:0xf bank_mask:0xa
	v_exp_f32_e32 v200, v168
	v_mov_b32_dpp v171, v175 quad_perm:[0,1,2,3] row_mask:0xf bank_mask:0xa
	v_exp_f32_e32 v201, v169
	v_exp_f32_e32 v202, v170
	v_add_f32_e32 v200, 1.0, v200
	v_exp_f32_e32 v203, v171
	v_add_f32_e32 v201, 1.0, v201
	v_add_f32_e32 v202, 1.0, v202
	v_rcp_f32_e32 v202, v202
	v_rcp_f32_e32 v200, v200
	v_rcp_f32_e32 v201, v201
	v_add_f32_e32 v203, 1.0, v203
	v_fmamk_f32 v204, v202, 0xc0b8aa3b, v222
	v_rcp_f32_e32 v203, v203
	v_mul_f32_e32 v205, v200, v204
	v_fma_f32 v220, v201, v220, v205
	v_exp_f32_e32 v206, v220
	v_mul_f32_e32 v207, -2.0, v203
	v_add_f32_e32 v206, 1.0, v206
	v_rcp_f32_e32 v206, v206
	s_nop 0
	v_fma_mixlo_f16 v208, v206, v207, v203
	ds_write_b16 v225, v208 offset:0
	v_fma_f32 v215, v206, v207, v203
	v_mfma_f32_16x16x32_f16 v[236:239], v[96:99], v[128:131], v[124:127]
	v_mfma_f32_16x16x32_f16 v[232:235], v[88:91], v[136:139], v[232:235]
	global_load_dwordx4 v[128:131], v[228:229], off offset:0
	ds_write_b128 v227, v[164:167] offset:64
	ds_read_b128 v[192:195], v226 offset:6528
	s_waitcnt lgkmcnt(2)
	s_barrier
	ds_read_b128 v[184:187], v209 offset:0
	ds_read_b128 v[188:191], v209 offset:64
	ds_read_b128 v[176:179], v211 offset:0
	ds_read_b128 v[180:183], v211 offset:64
	v_mfma_f32_16x16x32_f16 v[236:239], v[100:103], v[132:135], v[236:239]
	v_mfma_f32_16x16x32_f16 v[232:235], v[92:95], v[140:143], v[232:235]
	global_load_dwordx4 v[132:135], v[228:229], off offset:64
	s_waitcnt lgkmcnt(3)
	v_mfma_f32_16x16x32_f16 v[168:171], v[16:19], v[184:187], v[192:195]
	v_mfma_f32_16x16x32_f16 v[172:175], v[24:27], v[184:187], v[192:195]
	s_waitcnt lgkmcnt(2)
	v_mfma_f32_16x16x32_f16 v[168:171], v[20:23], v[188:191], v[168:171]
	v_mfma_f32_16x16x32_f16 v[172:175], v[28:31], v[188:191], v[172:175]
	s_waitcnt lgkmcnt(1)
	v_mfma_f32_16x16x32_f16 v[168:171], v[32:35], v[176:179], v[168:171]
	v_mfma_f32_16x16x32_f16 v[172:175], v[40:43], v[176:179], v[172:175]
	s_waitcnt lgkmcnt(0)
	v_mfma_f32_16x16x32_f16 v[168:171], v[36:39], v[180:183], v[168:171]
	v_mfma_f32_16x16x32_f16 v[172:175], v[44:47], v[180:183], v[172:175]
	v_max_f32_e32 v221, v221, v215
	s_nop 6
	v_mov_b32_dpp v168, v172 quad_perm:[0,1,2,3] row_mask:0xf bank_mask:0xa
	v_mov_b32_dpp v169, v173 quad_perm:[0,1,2,3] row_mask:0xf bank_mask:0xa
	v_mov_b32_dpp v170, v174 quad_perm:[0,1,2,3] row_mask:0xf bank_mask:0xa
	v_exp_f32_e32 v200, v168
	v_mov_b32_dpp v171, v175 quad_perm:[0,1,2,3] row_mask:0xf bank_mask:0xa
	v_exp_f32_e32 v201, v169
	v_exp_f32_e32 v202, v170
	v_add_f32_e32 v200, 1.0, v200
	v_exp_f32_e32 v203, v171
	v_add_f32_e32 v201, 1.0, v201
	v_add_f32_e32 v202, 1.0, v202
	v_rcp_f32_e32 v202, v202
	v_rcp_f32_e32 v200, v200
	v_rcp_f32_e32 v201, v201
	v_add_f32_e32 v203, 1.0, v203
	v_fmamk_f32 v204, v202, 0xc0b8aa3b, v222
	v_rcp_f32_e32 v203, v203
	v_mul_f32_e32 v205, v200, v204
	v_fma_f32 v220, v201, v220, v205
	v_exp_f32_e32 v206, v220
	v_mul_f32_e32 v207, -2.0, v203
	v_add_f32_e32 v206, 1.0, v206
	v_rcp_f32_e32 v206, v206
	s_nop 0
	v_fma_mixlo_f16 v208, v206, v207, v203
	ds_write_b16 v225, v208 offset:576
	v_fma_f32 v215, v206, v207, v203
	s_waitcnt vmcnt(5)
	v_mfma_f32_16x16x32_f16 v[160:163], v[48:51], v[144:147], v[112:115]
	v_mfma_f32_16x16x32_f16 v[236:239], v[104:107], v[136:139], v[236:239]
	global_load_dwordx4 v[136:139], v[228:229], off offset:128
	ds_write_b128 v227, v[232:235] offset:128
	ds_read_b128 v[196:199], v226 offset:7616
	s_waitcnt lgkmcnt(2)
	s_barrier
	ds_read_b128 v[184:187], v210 offset:576
	ds_read_b128 v[188:191], v210 offset:640
	ds_read_b128 v[176:179], v212 offset:576
	ds_read_b128 v[180:183], v212 offset:640
	s_waitcnt vmcnt(5)
	v_mfma_f32_16x16x32_f16 v[160:163], v[52:55], v[148:151], v[160:163]
	v_mfma_f32_16x16x32_f16 v[236:239], v[108:111], v[140:143], v[236:239]
	global_load_dwordx4 v[140:143], v[228:229], off offset:192
	v_lshl_add_u64 v[228:229], v[228:229], 0, s[20:21]
	s_waitcnt lgkmcnt(3)
	v_mfma_f32_16x16x32_f16 v[168:171], v[16:19], v[184:187], v[196:199]
	v_mfma_f32_16x16x32_f16 v[172:175], v[24:27], v[184:187], v[196:199]
	s_waitcnt lgkmcnt(2)
	v_mfma_f32_16x16x32_f16 v[168:171], v[20:23], v[188:191], v[168:171]
	v_mfma_f32_16x16x32_f16 v[172:175], v[28:31], v[188:191], v[172:175]
	s_waitcnt lgkmcnt(1)
	v_mfma_f32_16x16x32_f16 v[168:171], v[32:35], v[176:179], v[168:171]
	v_mfma_f32_16x16x32_f16 v[172:175], v[40:43], v[176:179], v[172:175]
	s_waitcnt lgkmcnt(0)
	v_mfma_f32_16x16x32_f16 v[168:171], v[36:39], v[180:183], v[168:171]
	v_mfma_f32_16x16x32_f16 v[172:175], v[44:47], v[180:183], v[172:175]
	v_max_f32_e32 v221, v221, v215
	s_nop 6
	v_mov_b32_dpp v168, v172 quad_perm:[0,1,2,3] row_mask:0xf bank_mask:0xa
	v_mov_b32_dpp v169, v173 quad_perm:[0,1,2,3] row_mask:0xf bank_mask:0xa
	v_mov_b32_dpp v170, v174 quad_perm:[0,1,2,3] row_mask:0xf bank_mask:0xa
	v_exp_f32_e32 v200, v168
	v_mov_b32_dpp v171, v175 quad_perm:[0,1,2,3] row_mask:0xf bank_mask:0xa
	v_exp_f32_e32 v201, v169
	v_exp_f32_e32 v202, v170
	v_add_f32_e32 v200, 1.0, v200
	v_exp_f32_e32 v203, v171
	v_add_f32_e32 v201, 1.0, v201
	v_add_f32_e32 v202, 1.0, v202
	v_rcp_f32_e32 v202, v202
	v_rcp_f32_e32 v200, v200
	v_rcp_f32_e32 v201, v201
	v_add_f32_e32 v203, 1.0, v203
	v_fmamk_f32 v204, v202, 0xc0b8aa3b, v222
	v_rcp_f32_e32 v203, v203
	v_mul_f32_e32 v205, v200, v204
	v_fma_f32 v220, v201, v220, v205
	v_exp_f32_e32 v206, v220
	v_mul_f32_e32 v207, -2.0, v203
	v_add_f32_e32 v206, 1.0, v206
	v_rcp_f32_e32 v206, v206
	s_nop 0
	v_fma_mixlo_f16 v208, v206, v207, v203
	ds_write_b16 v225, v208 offset:0
	v_fma_f32 v215, v206, v207, v203
	v_mfma_f32_16x16x32_f16 v[164:167], v[64:67], v[144:147], v[116:119]
	s_waitcnt vmcnt(5)
	v_mfma_f32_16x16x32_f16 v[160:163], v[56:59], v[152:155], v[160:163]
	ds_write_b128 v227, v[236:239] offset:192
	ds_read_b128 v[192:195], v226 offset:0
	s_waitcnt lgkmcnt(2)
	s_barrier
	s_sub_u32 s4, s4, 1
	s_cmp_lg_u32 s4, 0
	s_cbranch_scc1 .Llstm3_loop
	v_max_f32_e32 v221, v221, v215
	global_store_dword v230, v221, s[12:13]
	s_endpgm
